# v21 + diff loop copy 1: tile-base select as one SCC branch instead of hipcc's vcc/exec branch ladder (7.12)
# speedup vs baseline: 1.0047x; 1.0047x over previous
; #define DMA_WAIT(last) do { if (last) asm volatile("s_waitcnt vmcnt(0)" ::: "memory"); else asm volatile("s_waitcnt vmcnt(%0)" :: "n"(NPW) : "memory"); } while (0)
; template <int DK, int DV, bool OFF, class QLoader> ...
;     ...
;   f32x16 pA0, pA1, pB0, pB1; bf16x8 pa0, pa1, pa2, pa3; const int NT = nkeys / KVBLK;
;   DMA_TILE(0, 0); DMA_TILE(1, 1); DMA_WAIT(false); __syncthreads(); if (2 < NT) DMA_TILE(2, 2);
;   qkt<DK>(pA0, pA1, K_lds, qr, r32, hi); partialSM<DK, OFF>(pA0, pA1, negMC);
.LBB0_844:
.LBB0_846:
	s_add_i32 s28, s55, -3
	s_cmp_lt_u32 s28, s95
	s_cselect_b64 s[24:25], -1, 0
	s_cmp_ge_u32 s28, s95
	s_cselect_b64 s[28:29], -1, 0
	s_and_b64 vcc, exec, s[28:29]
	s_waitcnt vmcnt(0)
	s_barrier
	s_cbranch_vccnz .LBB0_856
	s_cmp_lg_u32 s80, 0
	s_cbranch_scc1 .LBB0_856
	s_cmp_gt_u32 s57, 1
	s_cbranch_scc0 .Lc1t_ctx
	s_lshl_b64 s[30:31], s[2:3], 7
	s_add_u32 s30, s93, s30
	s_addc_u32 s31, s94, s31
	s_mul_i32 s36, s2, 0x1800
	s_mul_hi_u32 s37, s2, 0x1800
	s_add_u32 s36, s74, s36
	s_addc_u32 s37, s75, s37
	s_branch .LBB0_855
